# baseline (speedup 1.0000x reference)
.LBB0_19:
	ds_read2_b32 v[36:37], v31 offset1:68
	ds_read_b128 v[32:35], v30
	ds_read_b128 v[40:43], v30 offset:16
	ds_read_b128 v[44:47], v30 offset:32
	ds_read_b128 v[48:51], v30 offset:48
	ds_read_b128 v[52:55], v30 offset:80
	ds_read_b128 v[56:59], v30 offset:96
	ds_read_b128 v[60:63], v30 offset:112
	ds_read_b128 v[64:67], v30 offset:128
	s_add_i32 s70, s70, 2
	s_waitcnt lgkmcnt(4)
	v_pk_fma_f32 v[16:17], v[34:35], v[36:37], v[16:17] op_sel_hi:[1,0,1]
	v_pk_fma_f32 v[12:13], v[42:43], v[36:37], v[12:13] op_sel_hi:[1,0,1]
	v_pk_fma_f32 v[8:9], v[46:47], v[36:37], v[8:9] op_sel_hi:[1,0,1]
	v_pk_fma_f32 v[0:1], v[50:51], v[36:37], v[0:1] op_sel_hi:[1,0,1]
	v_pk_fma_f32 v[18:19], v[32:33], v[36:37], v[18:19] op_sel_hi:[1,0,1]
	v_pk_fma_f32 v[14:15], v[40:41], v[36:37], v[14:15] op_sel_hi:[1,0,1]
	v_pk_fma_f32 v[10:11], v[44:45], v[36:37], v[10:11] op_sel_hi:[1,0,1]
	v_pk_fma_f32 v[6:7], v[48:49], v[36:37], v[6:7] op_sel_hi:[1,0,1]
	v_mov_b32_e32 v32, v37
	v_add_u32_e32 v31, 0x220, v31
	v_add_u32_e32 v30, 0xa0, v30
	s_cmp_eq_u32 s72, s70
	s_waitcnt lgkmcnt(0)
	v_pk_fma_f32 v[0:1], v[66:67], v[32:33], v[0:1] op_sel_hi:[1,0,1]
	v_pk_fma_f32 v[8:9], v[62:63], v[32:33], v[8:9] op_sel_hi:[1,0,1]
	v_pk_fma_f32 v[12:13], v[58:59], v[32:33], v[12:13] op_sel_hi:[1,0,1]
	v_pk_fma_f32 v[16:17], v[54:55], v[32:33], v[16:17] op_sel_hi:[1,0,1]
	v_pk_fma_f32 v[6:7], v[64:65], v[32:33], v[6:7] op_sel_hi:[1,0,1]
	v_pk_fma_f32 v[10:11], v[60:61], v[32:33], v[10:11] op_sel_hi:[1,0,1]
	v_pk_fma_f32 v[14:15], v[56:57], v[32:33], v[14:15] op_sel_hi:[1,0,1]
	v_pk_fma_f32 v[18:19], v[52:53], v[32:33], v[18:19] op_sel_hi:[1,0,1]
	s_cbranch_scc0 .LBB0_19
	s_mov_b32 s70, s72
	s_andn2_b64 vcc, exec, s[64:65]
	s_cbranch_vccz .LBB0_26
	s_branch .LBB0_27

_Z11attn_kernelPKfiPDF16_S1_iii:
	s_load_dwordx4 s[20:23], s[0:1], 0x20
	v_mov_b32_e32 v1, 0x2200
	v_lshl_or_b32 v1, v0, 2, v1
	s_mov_b32 s11, 0
	s_waitcnt lgkmcnt(0)
	s_cmp_gt_i32 s20, 0
	s_cselect_b64 s[28:29], -1, 0
	s_cmp_lt_i32 s20, 1
	s_cbranch_scc1 .LBB4_11
	s_load_dword s10, s[0:1], 0x8
	s_load_dwordx2 s[4:5], s[0:1], 0x0
	v_lshlrev_b32_e32 v2, 2, v0
	v_add_u32_e32 v3, 0x1000, v2
	s_waitcnt lgkmcnt(0)
	s_mul_i32 s10, s10, s2
	s_mul_i32 s10, s10, 0x1800
	s_lshl_b32 s6, s3, 8
	s_add_u32 s10, s10, s6
	s_add_u32 s40, s4, s10
	s_addc_u32 s41, s5, 0
	global_load_dword v50, v2, s[40:41]
	global_load_dword v51, v2, s[40:41] offset:2048
	global_load_dword v52, v3, s[40:41]
	s_cmp_le_i32 s20, 1
	s_cbranch_scc1 .Lattn_fill_wait
	s_add_u32 s40, s40, 0x1800
	s_addc_u32 s41, s41, 0
	global_load_dword v53, v2, s[40:41]
	global_load_dword v54, v2, s[40:41] offset:2048
	global_load_dword v55, v3, s[40:41]
	s_cmp_le_i32 s20, 2
	s_cbranch_scc1 .Lattn_fill_wait
	s_add_u32 s40, s40, 0x1800
	s_addc_u32 s41, s41, 0
	global_load_dword v56, v2, s[40:41]
	global_load_dword v57, v2, s[40:41] offset:2048
	global_load_dword v58, v3, s[40:41]
	s_cmp_le_i32 s20, 3
	s_cbranch_scc1 .Lattn_fill_wait
	s_add_u32 s40, s40, 0x1800
	s_addc_u32 s41, s41, 0
	global_load_dword v59, v2, s[40:41]
	global_load_dword v60, v2, s[40:41] offset:2048
	global_load_dword v61, v3, s[40:41]
	s_cmp_le_i32 s20, 4
	s_cbranch_scc1 .Lattn_fill_wait
	s_add_u32 s40, s40, 0x1800
	s_addc_u32 s41, s41, 0
	global_load_dword v62, v2, s[40:41]
	global_load_dword v63, v2, s[40:41] offset:2048
	global_load_dword v64, v3, s[40:41]
	s_cmp_le_i32 s20, 5
	s_cbranch_scc1 .Lattn_fill_wait
	s_add_u32 s40, s40, 0x1800
	s_addc_u32 s41, s41, 0
	global_load_dword v65, v2, s[40:41]
	global_load_dword v66, v2, s[40:41] offset:2048
	global_load_dword v67, v3, s[40:41]
	s_cmp_le_i32 s20, 6
	s_cbranch_scc1 .Lattn_fill_wait
	s_add_u32 s40, s40, 0x1800
	s_addc_u32 s41, s41, 0
	global_load_dword v68, v2, s[40:41]
	global_load_dword v69, v2, s[40:41] offset:2048
	global_load_dword v70, v3, s[40:41]
	s_cmp_le_i32 s20, 7
	s_cbranch_scc1 .Lattn_fill_wait
	s_add_u32 s40, s40, 0x1800
	s_addc_u32 s41, s41, 0
	global_load_dword v71, v2, s[40:41]
	global_load_dword v72, v2, s[40:41] offset:2048
	global_load_dword v73, v3, s[40:41]
	s_cmp_le_i32 s20, 8
	s_cbranch_scc1 .Lattn_fill_wait
	s_add_u32 s40, s40, 0x1800
	s_addc_u32 s41, s41, 0
	global_load_dword v74, v2, s[40:41]
	global_load_dword v75, v2, s[40:41] offset:2048
	global_load_dword v76, v3, s[40:41]
	s_cmp_le_i32 s20, 9
	s_cbranch_scc1 .Lattn_fill_wait
	s_add_u32 s40, s40, 0x1800
	s_addc_u32 s41, s41, 0
	global_load_dword v77, v2, s[40:41]
	global_load_dword v78, v2, s[40:41] offset:2048
	global_load_dword v79, v3, s[40:41]
	s_cmp_le_i32 s20, 10
	s_cbranch_scc1 .Lattn_fill_wait
	s_add_u32 s40, s40, 0x1800
	s_addc_u32 s41, s41, 0
	global_load_dword v80, v2, s[40:41]
	global_load_dword v81, v2, s[40:41] offset:2048
	global_load_dword v82, v3, s[40:41]
	s_cmp_le_i32 s20, 11
	s_cbranch_scc1 .Lattn_fill_wait
	s_add_u32 s40, s40, 0x1800
	s_addc_u32 s41, s41, 0
	global_load_dword v83, v2, s[40:41]
	global_load_dword v84, v2, s[40:41] offset:2048
	global_load_dword v85, v3, s[40:41]
	s_cmp_le_i32 s20, 12
	s_cbranch_scc1 .Lattn_fill_wait
	s_add_u32 s40, s40, 0x1800
	s_addc_u32 s41, s41, 0
	global_load_dword v86, v2, s[40:41]
	global_load_dword v87, v2, s[40:41] offset:2048
	global_load_dword v88, v3, s[40:41]
	s_cmp_le_i32 s20, 13
	s_cbranch_scc1 .Lattn_fill_wait
	s_add_u32 s40, s40, 0x1800
	s_addc_u32 s41, s41, 0
	global_load_dword v89, v2, s[40:41]
	global_load_dword v90, v2, s[40:41] offset:2048
	global_load_dword v91, v3, s[40:41]
	s_cmp_le_i32 s20, 14
	s_cbranch_scc1 .Lattn_fill_wait
	s_add_u32 s40, s40, 0x1800
	s_addc_u32 s41, s41, 0
	global_load_dword v92, v2, s[40:41]
	global_load_dword v93, v2, s[40:41] offset:2048
	global_load_dword v94, v3, s[40:41]
	s_cmp_le_i32 s20, 15
	s_cbranch_scc1 .Lattn_fill_wait
	s_add_u32 s40, s40, 0x1800
	s_addc_u32 s41, s41, 0
	global_load_dword v95, v2, s[40:41]
	global_load_dword v96, v2, s[40:41] offset:2048
	global_load_dword v97, v3, s[40:41]
.Lattn_fill_wait:
	s_waitcnt vmcnt(0)
	ds_write_b32 v2, v51
	ds_write_b32 v2, v50 offset:4352
	ds_write_b32 v2, v52 offset:8704
	s_cmp_le_i32 s20, 1
	s_cbranch_scc1 .LBB4_11
	ds_write_b32 v2, v54 offset:272
	ds_write_b32 v2, v53 offset:4624
	ds_write_b32 v2, v55 offset:8976
	s_cmp_le_i32 s20, 2
	s_cbranch_scc1 .LBB4_11
	ds_write_b32 v2, v57 offset:544
	ds_write_b32 v2, v56 offset:4896
	ds_write_b32 v2, v58 offset:9248
	s_cmp_le_i32 s20, 3
	s_cbranch_scc1 .LBB4_11
	ds_write_b32 v2, v60 offset:816
	ds_write_b32 v2, v59 offset:5168
	ds_write_b32 v2, v61 offset:9520
	s_cmp_le_i32 s20, 4
	s_cbranch_scc1 .LBB4_11
	ds_write_b32 v2, v63 offset:1088
	ds_write_b32 v2, v62 offset:5440
	ds_write_b32 v2, v64 offset:9792
	s_cmp_le_i32 s20, 5
	s_cbranch_scc1 .LBB4_11
	ds_write_b32 v2, v66 offset:1360
	ds_write_b32 v2, v65 offset:5712
	ds_write_b32 v2, v67 offset:10064
	s_cmp_le_i32 s20, 6
	s_cbranch_scc1 .LBB4_11
	ds_write_b32 v2, v69 offset:1632
	ds_write_b32 v2, v68 offset:5984
	ds_write_b32 v2, v70 offset:10336
	s_cmp_le_i32 s20, 7
	s_cbranch_scc1 .LBB4_11
	ds_write_b32 v2, v72 offset:1904
	ds_write_b32 v2, v71 offset:6256
	ds_write_b32 v2, v73 offset:10608
	s_cmp_le_i32 s20, 8
	s_cbranch_scc1 .LBB4_11
	ds_write_b32 v2, v75 offset:2176
	ds_write_b32 v2, v74 offset:6528
	ds_write_b32 v2, v76 offset:10880
	s_cmp_le_i32 s20, 9
	s_cbranch_scc1 .LBB4_11
	ds_write_b32 v2, v78 offset:2448
	ds_write_b32 v2, v77 offset:6800
	ds_write_b32 v2, v79 offset:11152
	s_cmp_le_i32 s20, 10
	s_cbranch_scc1 .LBB4_11
	ds_write_b32 v2, v81 offset:2720
	ds_write_b32 v2, v80 offset:7072
	ds_write_b32 v2, v82 offset:11424
	s_cmp_le_i32 s20, 11
	s_cbranch_scc1 .LBB4_11
	ds_write_b32 v2, v84 offset:2992
	ds_write_b32 v2, v83 offset:7344
	ds_write_b32 v2, v85 offset:11696
	s_cmp_le_i32 s20, 12
	s_cbranch_scc1 .LBB4_11
	ds_write_b32 v2, v87 offset:3264
	ds_write_b32 v2, v86 offset:7616
	ds_write_b32 v2, v88 offset:11968
	s_cmp_le_i32 s20, 13
	s_cbranch_scc1 .LBB4_11
	ds_write_b32 v2, v90 offset:3536
	ds_write_b32 v2, v89 offset:7888
	ds_write_b32 v2, v91 offset:12240
	s_cmp_le_i32 s20, 14
	s_cbranch_scc1 .LBB4_11
	ds_write_b32 v2, v93 offset:3808
	ds_write_b32 v2, v92 offset:8160
	ds_write_b32 v2, v94 offset:12512
	s_cmp_le_i32 s20, 15
	s_cbranch_scc1 .LBB4_11
	ds_write_b32 v2, v96 offset:4080
	ds_write_b32 v2, v95 offset:8432
	ds_write_b32 v2, v97 offset:12784

.LBB4_61:
	s_cmp_gt_i32 s21, 15
	s_cselect_b64 s[6:7], -1, 0
	s_cmp_lt_i32 s20, 16
	s_cselect_b64 s[8:9], -1, 0
	s_or_b64 s[6:7], s[6:7], s[8:9]
	s_and_b64 vcc, exec, s[6:7]
	s_cbranch_vccnz .LBB4_63
	s_add_i32 s4, s4, 15
	s_and_b64 s[0:1], s[0:1], exec
	s_cselect_b32 s0, s4, s2
	s_ashr_i32 s1, s0, 31
	s_lshl_b64 s[0:1], s[0:1], 9
	s_mov_b32 s3, 0x43800000
	v_lshl_add_u64 v[0:1], v[0:1], 0, s[0:1]
	v_fma_mixlo_f16 v4, v3, s3, 0
	v_lshlrev_b64 v[0:1], 1, v[0:1]
	v_fma_mixlo_f16 v5, v3, s3, -v4 op_sel_hi:[0,0,1]
	v_lshl_add_u64 v[2:3], s[24:25], 0, v[0:1]
	v_lshl_add_u64 v[0:1], s[26:27], 0, v[0:1]
	global_store_short v[2:3], v4, off
	global_store_short v[0:1], v5, off
.LBB4_63:
	s_endpgm
	s_endpgm
	s_endpgm
	s_endpgm
	s_endpgm
	s_endpgm
	s_endpgm
	s_endpgm
	s_endpgm
	s_endpgm
	s_endpgm
	s_endpgm
	s_endpgm
	s_endpgm
	.section	.rodata,"a",@progbits
	.p2align	6, 0x0
